# baseline (speedup 1.0000x reference)
.Lk1_nowarm9:
	buffer_load_dword v8, v1, s[8:11], s40 offen nt
	buffer_load_dword v9, v1, s[8:11], s41 offen nt
	buffer_load_dword v10, v1, s[8:11], s42 offen nt
	buffer_load_dword v11, v1, s[8:11], s43 offen nt
	buffer_load_dword v12, v1, s[8:11], s44 offen nt
	buffer_load_dword v13, v1, s[8:11], s45 offen nt
	buffer_load_dword v14, v1, s[8:11], s46 offen nt
	buffer_load_dword v15, v1, s[8:11], s47 offen nt
	buffer_load_dword v16, v1, s[8:11], s48 offen nt
	buffer_load_dword v17, v1, s[8:11], s49 offen nt
	buffer_load_dword v18, v1, s[8:11], s50 offen nt
	buffer_load_dword v19, v1, s[8:11], s51 offen nt
	buffer_load_dword v20, v1, s[8:11], s52 offen nt
	buffer_load_dword v21, v1, s[8:11], s53 offen nt
	buffer_load_dword v22, v1, s[8:11], s54 offen nt
	buffer_load_dword v23, v1, s[8:11], s55 offen nt
	s_add_u32 s8, s8, 0x4e200
	s_addc_u32 s9, s9, 0
	buffer_load_dword v24, v1, s[8:11], s40 offen nt
	buffer_load_dword v25, v1, s[8:11], s41 offen nt
	buffer_load_dword v26, v1, s[8:11], s42 offen nt
	buffer_load_dword v27, v1, s[8:11], s43 offen nt
	buffer_load_dword v28, v1, s[8:11], s44 offen nt
	buffer_load_dword v29, v1, s[8:11], s45 offen nt
	buffer_load_dword v30, v1, s[8:11], s46 offen nt
	buffer_load_dword v31, v1, s[8:11], s47 offen nt
	buffer_load_dword v32, v1, s[8:11], s48 offen nt
	buffer_load_dword v33, v1, s[8:11], s49 offen nt
	buffer_load_dword v34, v1, s[8:11], s50 offen nt
	buffer_load_dword v35, v1, s[8:11], s51 offen nt
	buffer_load_dword v36, v1, s[8:11], s52 offen nt
	buffer_load_dword v37, v1, s[8:11], s53 offen nt
	buffer_load_dword v38, v1, s[8:11], s54 offen nt
	buffer_load_dword v39, v1, s[8:11], s55 offen nt
	s_add_u32 s8, s8, 0x4e200
	s_addc_u32 s9, s9, 0
	buffer_load_dword v40, v1, s[8:11], s40 offen nt
	buffer_load_dword v41, v1, s[8:11], s41 offen nt
	buffer_load_dword v42, v1, s[8:11], s42 offen nt
	buffer_load_dword v43, v1, s[8:11], s43 offen nt
	buffer_load_dword v44, v1, s[8:11], s44 offen nt
	buffer_load_dword v45, v1, s[8:11], s45 offen nt
	buffer_load_dword v46, v1, s[8:11], s46 offen nt
	buffer_load_dword v47, v1, s[8:11], s47 offen nt
	buffer_load_dword v48, v1, s[8:11], s48 offen nt
	buffer_load_dword v49, v1, s[8:11], s49 offen nt
	buffer_load_dword v50, v1, s[8:11], s50 offen nt
	buffer_load_dword v51, v1, s[8:11], s51 offen nt
	buffer_load_dword v52, v1, s[8:11], s52 offen nt
	buffer_load_dword v53, v1, s[8:11], s53 offen nt
	buffer_load_dword v54, v1, s[8:11], s54 offen nt
	buffer_load_dword v55, v1, s[8:11], s55 offen nt
	v_mul_u32_u24_e32 v3, 0x147b, v2
	v_lshrrev_b32_e32 v3, 19, v3
	v_mul_u32_u24_e32 v98, 0x64, v3
	v_sub_u32_e32 v98, v2, v98
	v_add_u32_e32 v3, -1, v3
	v_add_u32_e32 v98, -1, v98
	s_movk_i32 s17, 0x62
	v_cmp_gt_u32_e64 s[36:37], 48, v3
	v_cmp_gt_u32_e64 s[38:39], s17, v98
	s_mul_i32 s17, s15, 0x1388
	v_add_lshl_u32 v98, v2, s17, 3
	s_and_b64 s[36:37], s[36:37], s[38:39]
	s_waitcnt vmcnt(32)
	s_add_u32 s8, s8, 0x4e200
	s_addc_u32 s9, s9, 0
	buffer_load_dword v56, v1, s[8:11], s40 offen nt
	buffer_load_dword v57, v1, s[8:11], s41 offen nt
	buffer_load_dword v58, v1, s[8:11], s42 offen nt
	buffer_load_dword v59, v1, s[8:11], s43 offen nt
	buffer_load_dword v60, v1, s[8:11], s44 offen nt
	buffer_load_dword v61, v1, s[8:11], s45 offen nt
	buffer_load_dword v62, v1, s[8:11], s46 offen nt
	buffer_load_dword v63, v1, s[8:11], s47 offen nt
	buffer_load_dword v64, v1, s[8:11], s48 offen nt
	buffer_load_dword v65, v1, s[8:11], s49 offen nt
	buffer_load_dword v66, v1, s[8:11], s50 offen nt
	buffer_load_dword v67, v1, s[8:11], s51 offen nt
	buffer_load_dword v68, v1, s[8:11], s52 offen nt
	buffer_load_dword v69, v1, s[8:11], s53 offen nt
	buffer_load_dword v70, v1, s[8:11], s54 offen nt
	buffer_load_dword v71, v1, s[8:11], s55 offen nt
	s_add_u32 s8, s8, 0x4e200
	s_addc_u32 s9, s9, 0
	buffer_load_dword v72, v1, s[8:11], s40 offen nt
	v_max3_f32 v76, v8, v9, v10
	v_max3_f32 v76, v76, v11, v12
	v_max3_f32 v76, v76, v13, v14
	v_max3_f32 v76, v76, v15, v16
	v_max3_f32 v76, v76, v17, v18
	v_max3_f32 v76, v76, v19, v20
	v_max3_f32 v76, v76, v21, v22
	v_max_f32_e32 v76, v76, v23
	v_sub_f32_e32 v8, v8, v76
	v_sub_f32_e32 v9, v9, v76
	v_sub_f32_e32 v10, v10, v76
	v_sub_f32_e32 v11, v11, v76
	v_sub_f32_e32 v12, v12, v76
	v_sub_f32_e32 v13, v13, v76
	v_sub_f32_e32 v14, v14, v76
	v_sub_f32_e32 v15, v15, v76
	v_sub_f32_e32 v16, v16, v76
	v_sub_f32_e32 v17, v17, v76
	v_sub_f32_e32 v18, v18, v76
	v_sub_f32_e32 v19, v19, v76
	v_sub_f32_e32 v20, v20, v76
	v_sub_f32_e32 v21, v21, v76
	v_sub_f32_e32 v22, v22, v76
	v_sub_f32_e32 v23, v23, v76
	v_or_b32_e32 v81, 0, v8
	v_or_b32_e32 v82, 1, v9
	v_min_u32_e32 v80, v81, v82
	v_or_b32_e32 v81, 2, v10
	v_or_b32_e32 v82, 3, v11
	v_min3_u32 v80, v80, v81, v82
	v_or_b32_e32 v81, 4, v12
	v_or_b32_e32 v82, 5, v13
	v_min3_u32 v80, v80, v81, v82
	v_or_b32_e32 v81, 6, v14
	v_or_b32_e32 v82, 7, v15
	v_min3_u32 v80, v80, v81, v82
	v_or_b32_e32 v81, 8, v16
	v_or_b32_e32 v82, 9, v17
	v_min3_u32 v80, v80, v81, v82
	v_or_b32_e32 v81, 10, v18
	v_or_b32_e32 v82, 11, v19
	v_min3_u32 v80, v80, v81, v82
	v_or_b32_e32 v81, 12, v20
	v_or_b32_e32 v82, 13, v21
	v_min3_u32 v80, v80, v81, v82
	v_or_b32_e32 v81, 14, v22
	v_or_b32_e32 v82, 15, v23
	v_min3_u32 v80, v80, v81, v82
	v_mul_f32_e32 v8, s14, v8
	v_mul_f32_e32 v9, s14, v9
	v_mul_f32_e32 v10, s14, v10
	v_mul_f32_e32 v11, s14, v11
	v_mul_f32_e32 v12, s14, v12
	v_mul_f32_e32 v13, s14, v13
	v_mul_f32_e32 v14, s14, v14
	v_mul_f32_e32 v15, s14, v15
	v_mul_f32_e32 v16, s14, v16
	v_mul_f32_e32 v17, s14, v17
	v_mul_f32_e32 v18, s14, v18
	v_mul_f32_e32 v19, s14, v19
	v_mul_f32_e32 v20, s14, v20
	v_mul_f32_e32 v21, s14, v21
	v_mul_f32_e32 v22, s14, v22
	v_mul_f32_e32 v23, s14, v23
	v_exp_f32_e32 v8, v8
	v_exp_f32_e32 v9, v9
	v_exp_f32_e32 v10, v10
	v_exp_f32_e32 v11, v11
	v_exp_f32_e32 v12, v12
	v_exp_f32_e32 v13, v13
	v_exp_f32_e32 v14, v14
	v_exp_f32_e32 v15, v15
	v_exp_f32_e32 v16, v16
	v_exp_f32_e32 v17, v17
	v_exp_f32_e32 v18, v18
	v_exp_f32_e32 v19, v19
	v_exp_f32_e32 v20, v20
	v_exp_f32_e32 v21, v21
	v_exp_f32_e32 v22, v22
	v_exp_f32_e32 v23, v23
	v_add_f32_e32 v78, v8, v10
	v_add_f32_e32 v79, v9, v11
	v_add_f32_e32 v78, v78, v12
	v_add_f32_e32 v79, v79, v13
	v_add_f32_e32 v78, v78, v14
	v_add_f32_e32 v79, v79, v15
	v_add_f32_e32 v78, v78, v16
	v_add_f32_e32 v79, v79, v17
	v_add_f32_e32 v78, v78, v18
	v_add_f32_e32 v79, v79, v19
	v_add_f32_e32 v78, v78, v20
	v_add_f32_e32 v79, v79, v21
	v_add_f32_e32 v78, v78, v22
	v_add_f32_e32 v79, v79, v23
	v_add_f32_e32 v78, v78, v79
	v_cvt_f64_f32_e32 v[86:87], v78
	v_mov_b32_e32 v75, v80
	v_mov_b32_e32 v73, v76
	s_waitcnt vmcnt(33)
	v_max3_f32 v76, v24, v25, v26
	v_max3_f32 v76, v76, v27, v28
	v_max3_f32 v76, v76, v29, v30
	v_max3_f32 v76, v76, v31, v32
	v_max3_f32 v76, v76, v33, v34
	v_max3_f32 v76, v76, v35, v36
	v_max3_f32 v76, v76, v37, v38
	v_max_f32_e32 v76, v76, v39
	v_max_f32_e32 v77, v73, v76
	v_cmp_gt_f32_e64 s[26:27], v76, v73
	v_sub_f32_e32 v83, v73, v77
	v_mul_f32_e32 v83, s14, v83
	v_exp_f32_e32 v83, v83
	v_sub_f32_e32 v24, v24, v77
	v_sub_f32_e32 v25, v25, v77
	v_sub_f32_e32 v26, v26, v77
	v_sub_f32_e32 v27, v27, v77
	v_sub_f32_e32 v28, v28, v77
	v_sub_f32_e32 v29, v29, v77
	v_sub_f32_e32 v30, v30, v77
	v_sub_f32_e32 v31, v31, v77
	v_sub_f32_e32 v32, v32, v77
	v_sub_f32_e32 v33, v33, v77
	v_sub_f32_e32 v34, v34, v77
	v_sub_f32_e32 v35, v35, v77
	v_sub_f32_e32 v36, v36, v77
	v_sub_f32_e32 v37, v37, v77
	v_sub_f32_e32 v38, v38, v77
	v_sub_f32_e32 v39, v39, v77
	v_cvt_f64_f32_e32 v[84:85], v83
	v_or_b32_e32 v81, 16, v24
	v_or_b32_e32 v82, 17, v25
	v_min_u32_e32 v80, v81, v82
	v_or_b32_e32 v81, 18, v26
	v_or_b32_e32 v82, 19, v27
	v_min3_u32 v80, v80, v81, v82
	v_or_b32_e32 v81, 20, v28
	v_or_b32_e32 v82, 21, v29
	v_min3_u32 v80, v80, v81, v82
	v_or_b32_e32 v81, 22, v30
	v_or_b32_e32 v82, 23, v31
	v_min3_u32 v80, v80, v81, v82
	v_or_b32_e32 v81, 24, v32
	v_or_b32_e32 v82, 25, v33
	v_min3_u32 v80, v80, v81, v82
	v_or_b32_e32 v81, 26, v34
	v_or_b32_e32 v82, 27, v35
	v_min3_u32 v80, v80, v81, v82
	v_or_b32_e32 v81, 28, v36
	v_or_b32_e32 v82, 29, v37
	v_min3_u32 v80, v80, v81, v82
	v_or_b32_e32 v81, 30, v38
	v_or_b32_e32 v82, 31, v39
	v_min3_u32 v80, v80, v81, v82
	v_mul_f64 v[86:87], v[86:87], v[84:85]
	v_mul_f32_e32 v24, s14, v24
	v_mul_f32_e32 v25, s14, v25
	v_mul_f32_e32 v26, s14, v26
	v_mul_f32_e32 v27, s14, v27
	v_mul_f32_e32 v28, s14, v28
	v_mul_f32_e32 v29, s14, v29
	v_mul_f32_e32 v30, s14, v30
	v_mul_f32_e32 v31, s14, v31
	v_mul_f32_e32 v32, s14, v32
	v_mul_f32_e32 v33, s14, v33
	v_mul_f32_e32 v34, s14, v34
	v_mul_f32_e32 v35, s14, v35
	v_mul_f32_e32 v36, s14, v36
	v_mul_f32_e32 v37, s14, v37
	v_mul_f32_e32 v38, s14, v38
	v_mul_f32_e32 v39, s14, v39
	v_exp_f32_e32 v24, v24
	v_exp_f32_e32 v25, v25
	v_exp_f32_e32 v26, v26
	v_exp_f32_e32 v27, v27
	v_exp_f32_e32 v28, v28
	v_exp_f32_e32 v29, v29
	v_exp_f32_e32 v30, v30
	v_exp_f32_e32 v31, v31
	v_exp_f32_e32 v32, v32
	v_exp_f32_e32 v33, v33
	v_exp_f32_e32 v34, v34
	v_exp_f32_e32 v35, v35
	v_exp_f32_e32 v36, v36
	v_exp_f32_e32 v37, v37
	v_exp_f32_e32 v38, v38
	v_exp_f32_e32 v39, v39
	v_add_f32_e32 v78, v24, v26
	v_add_f32_e32 v79, v25, v27
	v_add_f32_e32 v78, v78, v28
	v_add_f32_e32 v79, v79, v29
	v_add_f32_e32 v78, v78, v30
	v_add_f32_e32 v79, v79, v31
	v_add_f32_e32 v78, v78, v32
	v_add_f32_e32 v79, v79, v33
	v_add_f32_e32 v78, v78, v34
	v_add_f32_e32 v79, v79, v35
	v_add_f32_e32 v78, v78, v36
	v_add_f32_e32 v79, v79, v37
	v_add_f32_e32 v78, v78, v38
	v_add_f32_e32 v79, v79, v39
	v_add_f32_e32 v78, v78, v79
	v_cvt_f64_f32_e32 v[84:85], v78
	v_cndmask_b32_e64 v75, v75, v80, s[26:27]
	v_mov_b32_e32 v73, v77
	v_add_f64 v[86:87], v[86:87], v[84:85]
	s_waitcnt vmcnt(17)
	v_max3_f32 v76, v40, v41, v42
	v_max3_f32 v76, v76, v43, v44
	v_max3_f32 v76, v76, v45, v46
	v_max3_f32 v76, v76, v47, v48
	v_max3_f32 v76, v76, v49, v50
	v_max3_f32 v76, v76, v51, v52
	v_max3_f32 v76, v76, v53, v54
	v_max_f32_e32 v76, v76, v55
	v_max_f32_e32 v77, v73, v76
	v_cmp_gt_f32_e64 s[26:27], v76, v73
	v_sub_f32_e32 v83, v73, v77
	v_mul_f32_e32 v83, s14, v83
	v_exp_f32_e32 v83, v83
	v_sub_f32_e32 v40, v40, v77
	v_sub_f32_e32 v41, v41, v77
	v_sub_f32_e32 v42, v42, v77
	v_sub_f32_e32 v43, v43, v77
	v_sub_f32_e32 v44, v44, v77
	v_sub_f32_e32 v45, v45, v77
	v_sub_f32_e32 v46, v46, v77
	v_sub_f32_e32 v47, v47, v77
	v_sub_f32_e32 v48, v48, v77
	v_sub_f32_e32 v49, v49, v77
	v_sub_f32_e32 v50, v50, v77
	v_sub_f32_e32 v51, v51, v77
	v_sub_f32_e32 v52, v52, v77
	v_sub_f32_e32 v53, v53, v77
	v_sub_f32_e32 v54, v54, v77
	v_sub_f32_e32 v55, v55, v77
	v_cvt_f64_f32_e32 v[84:85], v83
	v_or_b32_e32 v81, 32, v40
	v_or_b32_e32 v82, 33, v41
	v_min_u32_e32 v80, v81, v82
	v_or_b32_e32 v81, 34, v42
	v_or_b32_e32 v82, 35, v43
	v_min3_u32 v80, v80, v81, v82
	v_or_b32_e32 v81, 36, v44
	v_or_b32_e32 v82, 37, v45
	v_min3_u32 v80, v80, v81, v82
	v_or_b32_e32 v81, 38, v46
	v_or_b32_e32 v82, 39, v47
	v_min3_u32 v80, v80, v81, v82
	v_or_b32_e32 v81, 40, v48
	v_or_b32_e32 v82, 41, v49
	v_min3_u32 v80, v80, v81, v82
	v_or_b32_e32 v81, 42, v50
	v_or_b32_e32 v82, 43, v51
	v_min3_u32 v80, v80, v81, v82
	v_or_b32_e32 v81, 44, v52
	v_or_b32_e32 v82, 45, v53
	v_min3_u32 v80, v80, v81, v82
	v_or_b32_e32 v81, 46, v54
	v_or_b32_e32 v82, 47, v55
	v_min3_u32 v80, v80, v81, v82
	v_mul_f64 v[86:87], v[86:87], v[84:85]
	v_mul_f32_e32 v40, s14, v40
	v_mul_f32_e32 v41, s14, v41
	v_mul_f32_e32 v42, s14, v42
	v_mul_f32_e32 v43, s14, v43
	v_mul_f32_e32 v44, s14, v44
	v_mul_f32_e32 v45, s14, v45
	v_mul_f32_e32 v46, s14, v46
	v_mul_f32_e32 v47, s14, v47
	v_mul_f32_e32 v48, s14, v48
	v_mul_f32_e32 v49, s14, v49
	v_mul_f32_e32 v50, s14, v50
	v_mul_f32_e32 v51, s14, v51
	v_mul_f32_e32 v52, s14, v52
	v_mul_f32_e32 v53, s14, v53
	v_mul_f32_e32 v54, s14, v54
	v_mul_f32_e32 v55, s14, v55
	v_exp_f32_e32 v40, v40
	v_exp_f32_e32 v41, v41
	v_exp_f32_e32 v42, v42
	v_exp_f32_e32 v43, v43
	v_exp_f32_e32 v44, v44
	v_exp_f32_e32 v45, v45
	v_exp_f32_e32 v46, v46
	v_exp_f32_e32 v47, v47
	v_exp_f32_e32 v48, v48
	v_exp_f32_e32 v49, v49
	v_exp_f32_e32 v50, v50
	v_exp_f32_e32 v51, v51
	v_exp_f32_e32 v52, v52
	v_exp_f32_e32 v53, v53
	v_exp_f32_e32 v54, v54
	v_exp_f32_e32 v55, v55
	v_add_f32_e32 v78, v40, v42
	v_add_f32_e32 v79, v41, v43
	v_add_f32_e32 v78, v78, v44
	v_add_f32_e32 v79, v79, v45
	v_add_f32_e32 v78, v78, v46
	v_add_f32_e32 v79, v79, v47
	v_add_f32_e32 v78, v78, v48
	v_add_f32_e32 v79, v79, v49
	v_add_f32_e32 v78, v78, v50
	v_add_f32_e32 v79, v79, v51
	v_add_f32_e32 v78, v78, v52
	v_add_f32_e32 v79, v79, v53
	v_add_f32_e32 v78, v78, v54
	v_add_f32_e32 v79, v79, v55
	v_add_f32_e32 v78, v78, v79
	v_cvt_f64_f32_e32 v[84:85], v78
	v_cndmask_b32_e64 v75, v75, v80, s[26:27]
	v_mov_b32_e32 v73, v77
	v_add_f64 v[86:87], v[86:87], v[84:85]
	s_cmp_eq_u32 s21, 2
	s_cselect_b32 s17, 1, 0
	s_cmp_eq_u32 s16, 4
	s_cselect_b32 s17, s17, 0
	s_cmp_lg_u32 s17, 0
	s_cbranch_scc0 .Lk1_nopiv
	v_cvt_f32_f64_e32 v3, v[86:87]
	s_mov_b32 s22, 0
	v_rcp_f32_e32 v3, v3
	s_mov_b32 s23, 0x20000000
	v_mul_f32_e32 v3, 0x3f3d0bd1, v3
.Lk1_piv:
	s_or_b32 s24, s22, s23
	v_cmp_le_u32_e32 vcc, s24, v3
	s_lshr_b32 s23, s23, 1
	s_bcnt1_i32_b64 s25, vcc
	s_cmp_ge_u32 s25, 20
	s_cselect_b32 s22, s24, s22
	s_cmp_ge_u32 s23, 0x4000
	s_cbranch_scc1 .Lk1_piv
	s_lshl_b32 s23, s15, 2
	s_add_u32 s23, s23, 0x138800
	v_mov_b32_e32 v3, s23
	v_mov_b32_e32 v81, s22
	s_mov_b64 exec, 1
	global_store_dword v3, v81, s[6:7]
	s_mov_b64 exec, s[18:19]
.Lk1_nopiv:
	s_waitcnt vmcnt(9)
	v_max3_f32 v76, v56, v57, v58
	v_max3_f32 v76, v76, v59, v60
	v_max3_f32 v76, v76, v61, v62
	v_max_f32_e32 v76, v76, v63
	v_max_f32_e32 v77, v73, v76
	v_cmp_gt_f32_e64 s[26:27], v76, v73
	v_sub_f32_e32 v83, v73, v77
	v_mul_f32_e32 v83, s14, v83
	v_exp_f32_e32 v83, v83
	v_sub_f32_e32 v56, v56, v77
	v_sub_f32_e32 v57, v57, v77
	v_sub_f32_e32 v58, v58, v77
	v_sub_f32_e32 v59, v59, v77
	v_sub_f32_e32 v60, v60, v77
	v_sub_f32_e32 v61, v61, v77
	v_sub_f32_e32 v62, v62, v77
	v_sub_f32_e32 v63, v63, v77
	v_cvt_f64_f32_e32 v[84:85], v83
	v_or_b32_e32 v81, 48, v56
	v_or_b32_e32 v82, 49, v57
	v_min_u32_e32 v80, v81, v82
	v_or_b32_e32 v81, 50, v58
	v_or_b32_e32 v82, 51, v59
	v_min3_u32 v80, v80, v81, v82
	v_or_b32_e32 v81, 52, v60
	v_or_b32_e32 v82, 53, v61
	v_min3_u32 v80, v80, v81, v82
	v_or_b32_e32 v81, 54, v62
	v_or_b32_e32 v82, 55, v63
	v_min3_u32 v80, v80, v81, v82
	v_mul_f64 v[86:87], v[86:87], v[84:85]
	v_mul_f32_e32 v56, s14, v56
	v_mul_f32_e32 v57, s14, v57
	v_mul_f32_e32 v58, s14, v58
	v_mul_f32_e32 v59, s14, v59
	v_mul_f32_e32 v60, s14, v60
	v_mul_f32_e32 v61, s14, v61
	v_mul_f32_e32 v62, s14, v62
	v_mul_f32_e32 v63, s14, v63
	v_exp_f32_e32 v56, v56
	v_exp_f32_e32 v57, v57
	v_exp_f32_e32 v58, v58
	v_exp_f32_e32 v59, v59
	v_exp_f32_e32 v60, v60
	v_exp_f32_e32 v61, v61
	v_exp_f32_e32 v62, v62
	v_exp_f32_e32 v63, v63
	v_add_f32_e32 v78, v56, v58
	v_add_f32_e32 v79, v57, v59
	v_add_f32_e32 v78, v78, v60
	v_add_f32_e32 v79, v79, v61
	v_add_f32_e32 v78, v78, v62
	v_add_f32_e32 v79, v79, v63
	v_add_f32_e32 v78, v78, v79
	v_cvt_f64_f32_e32 v[84:85], v78
	v_cndmask_b32_e64 v75, v75, v80, s[26:27]
	v_mov_b32_e32 v73, v77
	v_add_f64 v[86:87], v[86:87], v[84:85]
	s_waitcnt vmcnt(4)
	v_max3_f32 v76, v64, v65, v66
	v_max3_f32 v76, v76, v67, v68
	v_max_f32_e32 v77, v73, v76
	v_cmp_gt_f32_e64 s[26:27], v76, v73
	v_sub_f32_e32 v83, v73, v77
	v_mul_f32_e32 v83, s14, v83
	v_exp_f32_e32 v83, v83
	v_sub_f32_e32 v64, v64, v77
	v_sub_f32_e32 v65, v65, v77
	v_sub_f32_e32 v66, v66, v77
	v_sub_f32_e32 v67, v67, v77
	v_sub_f32_e32 v68, v68, v77
	v_cvt_f64_f32_e32 v[84:85], v83
	v_or_b32_e32 v81, 56, v64
	v_or_b32_e32 v82, 57, v65
	v_min_u32_e32 v80, v81, v82
	v_or_b32_e32 v81, 58, v66
	v_or_b32_e32 v82, 59, v67
	v_min3_u32 v80, v80, v81, v82
	v_or_b32_e32 v81, 60, v68
	v_min_u32_e32 v80, v80, v81
	v_mul_f64 v[86:87], v[86:87], v[84:85]
	v_mul_f32_e32 v64, s14, v64
	v_mul_f32_e32 v65, s14, v65
	v_mul_f32_e32 v66, s14, v66
	v_mul_f32_e32 v67, s14, v67
	v_mul_f32_e32 v68, s14, v68
	v_exp_f32_e32 v64, v64
	v_exp_f32_e32 v65, v65
	v_exp_f32_e32 v66, v66
	v_exp_f32_e32 v67, v67
	v_exp_f32_e32 v68, v68
	v_add_f32_e32 v78, v64, v66
	v_add_f32_e32 v79, v65, v67
	v_add_f32_e32 v78, v78, v68
	v_add_f32_e32 v78, v78, v79
	v_cvt_f64_f32_e32 v[84:85], v78
	v_cndmask_b32_e64 v75, v75, v80, s[26:27]
	v_mov_b32_e32 v73, v77
	v_add_f64 v[86:87], v[86:87], v[84:85]
	s_waitcnt vmcnt(1)
	v_max3_f32 v76, v69, v70, v71
	v_max_f32_e32 v77, v73, v76
	v_cmp_gt_f32_e64 s[26:27], v76, v73
	v_sub_f32_e32 v83, v73, v77
	v_mul_f32_e32 v83, s14, v83
	v_exp_f32_e32 v83, v83
	v_sub_f32_e32 v69, v69, v77
	v_sub_f32_e32 v70, v70, v77
	v_sub_f32_e32 v71, v71, v77
	v_cvt_f64_f32_e32 v[84:85], v83
	v_or_b32_e32 v81, 61, v69
	v_or_b32_e32 v82, 62, v70
	v_min_u32_e32 v80, v81, v82
	v_or_b32_e32 v81, 63, v71
	v_min_u32_e32 v80, v80, v81
	v_mul_f64 v[86:87], v[86:87], v[84:85]
	v_mul_f32_e32 v69, s14, v69
	v_mul_f32_e32 v70, s14, v70
	v_mul_f32_e32 v71, s14, v71
	v_exp_f32_e32 v69, v69
	v_exp_f32_e32 v70, v70
	v_exp_f32_e32 v71, v71
	v_add_f32_e32 v78, v69, v70
	v_add_f32_e32 v78, v78, v71
	v_cvt_f64_f32_e32 v[84:85], v78
	v_cndmask_b32_e64 v75, v75, v80, s[26:27]
	v_mov_b32_e32 v73, v77
	v_add_f64 v[86:87], v[86:87], v[84:85]
	s_waitcnt vmcnt(0)
	v_max_f32_e32 v77, v73, v72
	v_cmp_gt_f32_e64 s[26:27], v72, v73
	v_sub_f32_e32 v83, v73, v77
	v_sub_f32_e32 v72, v72, v77
	v_mul_f32_e32 v83, s14, v83
	v_mul_f32_e32 v72, s14, v72
	v_exp_f32_e32 v83, v83
	v_exp_f32_e32 v72, v72
	v_cndmask_b32_e64 v75, v75, 64, s[26:27]
	v_cvt_f64_f32_e32 v[84:85], v83
	v_cvt_f64_f32_e32 v[90:91], v72
	v_mul_f64 v[86:87], v[86:87], v[84:85]
	v_add_f64 v[86:87], v[86:87], v[90:91]
	v_rcp_f64_e32 v[88:89], v[86:87]
	v_cmp_gt_u32_e32 vcc, 64, v75
	s_and_b64 vcc, vcc, s[36:37]
	v_fma_f64 v[90:91], -v[86:87], v[88:89], 1.0
	v_fma_f64 v[88:89], v[90:91], v[88:89], v[88:89]
	v_cvt_f32_f64_e32 v3, v[88:89]
	v_cndmask_b32_e32 v74, 0, v3, vcc
	global_store_dwordx2 v98, v[74:75], s[6:7]

.LBB1_74:
	s_or_b64 exec, exec, s[0:1]
	v_mov_b32_e32 v4, 0
	s_waitcnt lgkmcnt(0)
	s_barrier
	ds_read_b64 v[4:5], v4 offset:48432
	v_lshlrev_b32_e32 v6, 7, v0
	s_mov_b64 s[0:1], exec
	s_waitcnt lgkmcnt(0)
	v_cmp_ge_u32_e32 vcc, v14, v4
	s_and_b64 s[14:15], s[14:15], vcc
	v_cmp_le_u32_e32 vcc, s18, v2
	s_and_b64 s[14:15], s[14:15], vcc
	v_cmp_ge_u32_e32 vcc, v13, v4
	s_and_b64 s[12:13], s[12:13], vcc
	v_cmp_le_u32_e32 vcc, s18, v24
	s_and_b64 s[12:13], s[12:13], vcc
	v_cmp_ge_u32_e32 vcc, v12, v4
	s_and_b64 s[10:11], s[10:11], vcc
	v_cmp_le_u32_e32 vcc, s18, v22
	s_and_b64 s[10:11], s[10:11], vcc
	v_cmp_ge_u32_e32 vcc, v11, v4
	s_and_b64 s[6:7], s[6:7], vcc
	v_cmp_le_u32_e32 vcc, s18, v20
	s_and_b64 s[6:7], s[6:7], vcc
	v_cmp_ge_u32_e32 vcc, v10, v4
	s_and_b64 s[4:5], s[4:5], vcc
	v_cmp_le_u32_e32 vcc, s18, v18
	s_and_b64 s[4:5], s[4:5], vcc
	v_mov_b32_e32 v7, 1
	v_lshlrev_b32_e32 v14, 2, v14
	v_lshlrev_b32_e32 v13, 2, v13
	v_lshlrev_b32_e32 v12, 2, v12
	v_lshlrev_b32_e32 v11, 2, v11
	v_lshlrev_b32_e32 v10, 2, v10
	s_mov_b64 exec, s[14:15]
	ds_add_rtn_u32 v58, v14, v7
	s_mov_b64 exec, s[12:13]
	ds_add_rtn_u32 v59, v13, v7
	s_mov_b64 exec, s[10:11]
	ds_add_rtn_u32 v60, v12, v7
	s_mov_b64 exec, s[6:7]
	ds_add_rtn_u32 v61, v11, v7
	s_mov_b64 exec, s[4:5]
	ds_add_rtn_u32 v62, v10, v7
	s_mov_b64 exec, s[0:1]
	s_waitcnt lgkmcnt(0)
	v_sub_u32_e32 v8, 0xfff80, v6
	v_or_b32_e32 v8, v3, v8
	v_mov_b32_e32 v9, v2
	v_lshlrev_b32_e32 v58, 3, v58
	s_mov_b64 exec, s[14:15]
	ds_write_b64 v58, v[8:9] offset:8224
	s_mov_b64 exec, s[0:1]
	v_sub_u32_e32 v8, 0xdff80, v6
	v_or_b32_e32 v8, v25, v8
	v_mov_b32_e32 v9, v24
	v_lshlrev_b32_e32 v59, 3, v59
	s_mov_b64 exec, s[12:13]
	ds_write_b64 v59, v[8:9] offset:8224
	s_mov_b64 exec, s[0:1]
	v_sub_u32_e32 v8, 0xbff80, v6
	v_or_b32_e32 v8, v23, v8
	v_mov_b32_e32 v9, v22
	v_lshlrev_b32_e32 v60, 3, v60
	s_mov_b64 exec, s[10:11]
	ds_write_b64 v60, v[8:9] offset:8224
	s_mov_b64 exec, s[0:1]
	v_sub_u32_e32 v8, 0x9ff80, v6
	v_or_b32_e32 v8, v21, v8
	v_mov_b32_e32 v9, v20
	v_lshlrev_b32_e32 v61, 3, v61
	s_mov_b64 exec, s[6:7]
	ds_write_b64 v61, v[8:9] offset:8224
	s_mov_b64 exec, s[0:1]
	v_sub_u32_e32 v8, 0x7ff80, v6
	v_or_b32_e32 v8, v19, v8
	v_mov_b32_e32 v9, v18
	v_lshlrev_b32_e32 v62, 3, v62
	s_mov_b64 exec, s[4:5]
	ds_write_b64 v62, v[8:9] offset:8224
	s_mov_b64 exec, s[0:1]
	v_cmp_lt_i32_e32 vcc, v0, v5
	s_waitcnt lgkmcnt(0)
	s_barrier
	s_and_saveexec_b64 s[0:1], vcc
	s_cbranch_execz .LBB1_93
	s_mov_b64 s[2:3], 0
	s_movk_i32 s8, 0x12c
	s_mov_b32 s9, 0x51eb851f
	s_movk_i32 s10, 0xff9c
	s_mov_b32 s11, 0x43480000
	s_mov_b32 s12, 0x43c80000
	s_mov_b32 s13, 0x3ba3d70a
	s_mov_b32 s14, 0x3b23d70a
	v_mov_b32_e32 v4, 1.0
	v_mov_b32_e32 v10, 0x2020
	v_mov_b32_e32 v11, v0
	s_branch .LBB1_87
